# previous stack + MoE gate/up: next item's gathered-row indices requested early, one counted wait
# speedup vs baseline: 1.0164x; 1.0142x over previous
.LBB0_781:
	s_getreg_b32 s10, hwreg(HW_REG_HW_ID, 0, 6)
	s_lshl_b32 s10, s10, 2
	s_add_i32 s10, s10, 0x27000
	v_mov_b32_e32 v52, s10
	ds_read_b32 v52, v52
	v_cndmask_b32_e64 v177, 0, 1, s[18:19]
	v_mov_b32_e32 v53, v133
	v_readfirstlane_b32 s9, v177
	s_xor_b32 s47, s24, s9
	s_waitcnt lgkmcnt(0)
	v_readfirstlane_b32 s9, v52
	v_mbcnt_lo_u32_b32 v52, -1, v53
	v_mbcnt_hi_u32_b32 v52, -1, v52
	v_lshl_or_b32 v52, s9, 6, v52
	s_waitcnt vmcnt(7)
	v_cvt_pk_bf16_f32 v20, v20, v21
	v_lshrrev_b32_e32 v55, 3, v52
	v_lshlrev_b32_e32 v56, 4, v52
	v_and_b32_e32 v56, 0x70, v56
	v_mul_lo_u32 v55, v55, s29
	v_ashrrev_i32_e32 v54, 5, v52
	v_add3_u32 v57, 0, v56, v55
	ds_write_b128 v57, v[36:39]
	ds_write_b128 v57, v[32:35] offset:9216
	s_waitcnt vmcnt(6)
	ds_write_b128 v57, v[44:47] offset:18432
	s_waitcnt vmcnt(5)
	ds_write_b128 v57, v[40:43] offset:27648
	s_waitcnt vmcnt(4)
	ds_write_b128 v57, v[48:51] offset:36864
	v_lshrrev_b32_e32 v34, 1, v54
	v_bfe_u32 v32, v52, 2, 3
	v_and_b32_e32 v33, 3, v54
	v_and_b32_e32 v34, 4, v34
	v_bitop3_b32 v32, v34, v32, v33 bitop3:0x36
	v_lshlrev_b32_e32 v33, 2, v52
	v_and_b32_e32 v57, 12, v33
	v_lshlrev_b32_e32 v58, 1, v57
	v_lshl_or_b32 v59, v32, 5, v58
	v_lshlrev_b32_e32 v54, 8, v54
	v_cvt_pk_bf16_f32 v21, v22, v23
	v_add3_u32 v22, s33, v59, v54
	s_waitcnt vmcnt(6)
	v_cvt_pk_bf16_f32 v16, v16, v17
	v_cvt_pk_bf16_f32 v17, v18, v19
	ds_write2st64_b64 v22, v[20:21], v[16:17] offset1:8
	s_waitcnt vmcnt(5)
	v_cvt_pk_bf16_f32 v16, v28, v29
	v_cvt_pk_bf16_f32 v17, v30, v31
	s_waitcnt vmcnt(4)
	v_cvt_pk_bf16_f32 v18, v24, v25
	v_cvt_pk_bf16_f32 v19, v26, v27
	s_mul_i32 s9, s24, 0x2800
	ds_write2st64_b64 v22, v[16:17], v[18:19] offset0:16 offset1:24
	v_add_u32_e32 v16, s9, v174
	v_add_u32_e32 v217, s9, v168
	v_add_u32_e32 v218, 48, v16
	ds_read_b32 v132, v217
	ds_read2st64_b32 v[16:17], v218 offset0:20 offset1:28
	ds_read2st64_b32 v[22:23], v218 offset0:36 offset1:44
	v_bfe_u32 v25, v52, 2, 2
	v_bfe_u32 v26, v52, 6, 1
	s_waitcnt lgkmcnt(2)
	v_lshl_add_u64 v[18:19], v[132:133], 1, s[92:93]
	s_waitcnt lgkmcnt(1)
	v_mov_b32_e32 v132, v16
	v_lshl_add_u64 v[20:21], v[132:133], 1, s[92:93]
	v_mov_b32_e32 v132, v17
	v_lshl_add_u64 v[16:17], v[132:133], 1, s[92:93]
	s_waitcnt lgkmcnt(0)
	v_mov_b32_e32 v132, v22
	global_load_dwordx4 v[32:35], v[18:19], off offset:128
	global_load_dwordx4 v[36:39], v[20:21], off offset:128
	v_lshl_add_u64 v[18:19], v[132:133], 1, s[92:93]
	v_mov_b32_e32 v132, v23
	global_load_dwordx4 v[44:47], v[16:17], off offset:128
	global_load_dwordx4 v[48:51], v[18:19], off offset:128
	v_lshl_add_u64 v[16:17], v[132:133], 1, s[92:93]
	global_load_dwordx4 v[40:43], v[16:17], off offset:128
	v_lshrrev_b32_e32 v18, 2, v52
	v_and_b32_e32 v18, 4, v18
	v_lshrrev_b32_e32 v16, 1, v52
	v_or_b32_e32 v19, v18, v25
	v_and_b32_e32 v16, 24, v16
	v_lshlrev_b32_e32 v20, 6, v26
	v_lshlrev_b32_e32 v19, 4, v19
	v_lshlrev_b32_e32 v23, 2, v26
	v_or_b32_e32 v17, v16, v25
	v_xor_b32_e32 v19, v19, v20
	v_or_b32_e32 v26, 1, v23
	v_or_b32_e32 v27, 2, v23
	v_or_b32_e32 v23, 3, v23
	v_or_b32_e32 v19, v19, v57
	v_lshlrev_b32_e32 v17, 8, v17
	v_bitop3_b32 v26, v18, v26, v25 bitop3:0x36
	v_bitop3_b32 v27, v18, v27, v25 bitop3:0x36
	v_bitop3_b32 v18, v18, v23, v25 bitop3:0x36
	s_lshl_b32 s10, s7, 6
	v_ashrrev_i32_e32 v53, 7, v52
	v_add_u32_e32 v20, s33, v17
	v_lshlrev_b32_e32 v19, 1, v19
	v_lshl_or_b32 v26, v26, 5, v58
	v_lshl_or_b32 v27, v27, 5, v58
	v_lshl_or_b32 v18, v18, 5, v58
	s_ashr_i32 s11, s10, 31
	v_and_b32_e32 v24, 15, v52
	v_add_u32_e32 v213, v20, v19
	v_add_u32_e32 v214, v20, v26
	v_add_u32_e32 v211, v20, v27
	v_add_u32_e32 v145, v20, v18
	v_mul_lo_u32 v20, v53, s28
	s_cmpk_lt_i32 s8, 0x100
	v_add_u32_e32 v21, 0, v17
	v_or_b32_e32 v20, v20, v24
	s_cselect_b64 s[12:13], -1, 0
	s_cmpk_gt_i32 s8, 0xff
	v_add_u32_e32 v22, 0x16c00, v21
	v_lshlrev_b32_e32 v16, 1, v16
	v_mul_lo_u32 v20, v20, s29
	s_cselect_b64 s[14:15], -1, 0
	s_ashr_i32 s9, s8, 31
	v_add_u32_e32 v216, v22, v19
	v_add_u32_e32 v215, v22, v26
	v_add_u32_e32 v212, v22, v27
	v_add_u32_e32 v147, v22, v18
	v_add3_u32 v178, 0, v16, v20
	v_add3_u32 v16, 0, v54, v59
	v_add_u32_e32 v22, 0x18c00, v21
	s_lshl_b64 s[16:17], s[8:9], 16
	v_add_u32_e32 v209, 0x1b800, v16
	v_add_u32_e32 v208, 0x1c800, v16
	v_add_u32_e32 v206, 0x1d800, v16
	v_or_b32_e32 v20, 0x2000, v17
	v_add_u32_e32 v207, v22, v19
	v_add_u32_e32 v204, v22, v26
	v_add_u32_e32 v201, v22, v27
	v_add_u32_e32 v199, v22, v18
	v_add_u32_e32 v22, 0x1ac00, v21
	v_add_u32_e32 v220, 0x17800, v16
	v_add_u32_e32 v221, 0x18800, v16
	v_add_u32_e32 v222, 0x19800, v16
	v_add_u32_e32 v16, 0x1cc00, v21
	s_cmpk_lt_i32 s6, 0x100
	v_add_u32_e32 v21, s46, v141
	v_readlane_b32 s76, v253, 4
	v_add3_u32 v205, s33, v19, v20
	v_add3_u32 v203, s33, v26, v20
	v_add3_u32 v200, s33, v27, v20
	v_add3_u32 v198, s33, v18, v20
	v_add_u32_e32 v17, s42, v17
	v_add_u32_e32 v194, v22, v19
	v_add_u32_e32 v191, v22, v26
	v_add_u32_e32 v189, v22, v27
	v_add_u32_e32 v188, v22, v18
	v_add3_u32 v185, s42, v19, v20
	v_add3_u32 v183, s42, v26, v20
	v_add3_u32 v181, s42, v27, v20
	v_add3_u32 v179, s42, v18, v20
	v_add_u32_e32 v20, -1, v176
	v_add_u32_e32 v22, 0x80, v21
	s_cselect_b32 s20, s6, 0
	v_readlane_b32 s78, v253, 6
	v_readlane_b32 s79, v253, 7
	v_readlane_b32 s80, v253, 8
	v_readlane_b32 s81, v253, 9
	v_readlane_b32 s84, v253, 12
	v_readlane_b32 s85, v253, 13
	v_readlane_b32 s86, v253, 14
	v_readlane_b32 s87, v253, 15
	v_add_u32_e32 v187, v17, v18
	v_add_u32_e32 v186, v16, v19
	v_add_u32_e32 v184, v16, v26
	v_add_u32_e32 v182, v16, v27
	v_add_u32_e32 v180, v16, v18
	v_min_i32_e32 v16, v21, v20
	v_add_u32_e32 v18, 64, v21
	v_min_i32_e32 v148, v22, v20
	v_add_u32_e32 v22, 0xc0, v21
	v_add_u32_e32 v21, 0x100, v21
	s_cselect_b32 s50, s78, s84
	s_cselect_b32 s51, s79, s85
	s_cselect_b32 s52, s80, s86
	s_cselect_b32 s53, s81, s87
	s_ashr_i32 s21, s20, 31
	v_min_i32_e32 v150, v22, v20
	v_min_i32_e32 v152, v21, v20
	s_lshl_b64 s[20:21], s[20:21], 20
	v_mov_b32_e32 v21, s51
	v_mov_b32_e32 v22, s50
	v_readlane_b32 s50, v253, 61
	v_min_i32_e32 v18, v18, v20
	v_readlane_b32 s51, v253, 62
	s_add_u32 s16, s50, s16
	v_add_u32_e32 v193, v17, v19
	v_add_u32_e32 v190, v17, v26
	v_add_u32_e32 v192, v17, v27
	v_ashrrev_i32_e32 v17, 31, v16
	v_ashrrev_i32_e32 v19, 31, v18
	v_ashrrev_i32_e32 v149, 31, v148
	v_ashrrev_i32_e32 v151, 31, v150
	v_ashrrev_i32_e32 v153, 31, v152
	v_mov_b32_e32 v20, s53
	s_addc_u32 s17, s51, s17
	v_cndmask_b32_e64 v21, v20, v21, s[4:5]
	v_mov_b32_e32 v20, s52
	v_lshl_add_u64 v[154:155], v[16:17], 2, s[16:17]
	v_lshl_add_u64 v[156:157], v[18:19], 2, s[16:17]
	v_lshl_add_u64 v[158:159], v[148:149], 2, s[16:17]
	v_lshl_add_u64 v[160:161], v[150:151], 2, s[16:17]
	v_lshl_add_u64 v[162:163], v[152:153], 2, s[16:17]
	s_and_b64 s[98:99], s[18:19], s[12:13]
	s_cbranch_scc0 .Lopt1_m10_skip
	global_load_dword v224, v[154:155], off
	global_load_dword v225, v[156:157], off
	global_load_dword v226, v[158:159], off
	global_load_dword v227, v[160:161], off
	global_load_dword v228, v[162:163], off
.Lopt1_m10_skip:
	s_lshl_b64 s[16:17], s[10:11], 2
	v_cndmask_b32_e64 v20, v20, v22, s[4:5]
	s_add_u32 s16, s20, s16
	v_add3_u32 v195, 0, v55, v56
	s_mul_i32 s48, s47, 0x2800
	v_lshl_or_b32 v149, v16, 10, v167
	v_lshl_add_u64 v[16:17], v[20:21], 0, v[142:143]
	s_addc_u32 s17, s21, s17
	v_mov_b32_e32 v56, 0
	s_mov_b32 s49, 0
	v_add3_u32 v210, s42, v54, v59
	v_add_u32_e32 v196, 0x12000, v195
	v_add_u32_e32 v197, 0x14400, v195
	v_add3_u32 v219, s33, v54, v59
	v_add_u32_e32 v202, s48, v168
	v_lshl_or_b32 v151, v18, 10, v167
	v_lshl_add_u64 v[164:165], v[16:17], 0, s[16:17]
	s_mov_b64 s[16:17], 0
	s_xor_b64 s[18:19], s[18:19], -1
	v_mov_b32_e32 v57, v56
	v_mov_b32_e32 v58, v56
	v_mov_b32_e32 v59, v56
	v_mov_b32_e32 v72, v56
	v_mov_b32_e32 v73, v56
	v_mov_b32_e32 v74, v56
	v_mov_b32_e32 v75, v56
	v_mov_b32_e32 v80, v56
	v_mov_b32_e32 v81, v56
	v_mov_b32_e32 v82, v56
	v_mov_b32_e32 v83, v56
	v_mov_b32_e32 v84, v56
	v_mov_b32_e32 v85, v56
	v_mov_b32_e32 v86, v56
	v_mov_b32_e32 v87, v56
	v_mov_b32_e32 v76, v56
	v_mov_b32_e32 v77, v56
	v_mov_b32_e32 v78, v56
	v_mov_b32_e32 v79, v56
	v_mov_b32_e32 v68, v56
	v_mov_b32_e32 v69, v56
	v_mov_b32_e32 v70, v56
	v_mov_b32_e32 v71, v56
	v_mov_b32_e32 v60, v56
	v_mov_b32_e32 v61, v56
	v_mov_b32_e32 v62, v56
	v_mov_b32_e32 v63, v56
	v_mov_b32_e32 v52, v56
	v_mov_b32_e32 v53, v56
	v_mov_b32_e32 v54, v56
	v_mov_b32_e32 v55, v56
	v_mov_b32_e32 v64, v56
	v_mov_b32_e32 v65, v56
	v_mov_b32_e32 v66, v56
	v_mov_b32_e32 v67, v56
	v_mov_b32_e32 v24, v56
	v_mov_b32_e32 v25, v56
	v_mov_b32_e32 v26, v56
	v_mov_b32_e32 v27, v56
	v_mov_b32_e32 v28, v56
	v_mov_b32_e32 v29, v56
	v_mov_b32_e32 v30, v56
	v_mov_b32_e32 v31, v56
	v_mov_b32_e32 v88, v56
	v_mov_b32_e32 v89, v56
	v_mov_b32_e32 v90, v56
	v_mov_b32_e32 v91, v56
	v_mov_b32_e32 v16, v56
	v_mov_b32_e32 v17, v56
	v_mov_b32_e32 v18, v56
	v_mov_b32_e32 v19, v56
	v_mov_b32_e32 v20, v56
	v_mov_b32_e32 v21, v56
	v_mov_b32_e32 v22, v56
	v_mov_b32_e32 v23, v56
	v_mov_b32_e32 v92, v56
	v_mov_b32_e32 v93, v56
	v_mov_b32_e32 v94, v56
	v_mov_b32_e32 v95, v56
	v_mov_b32_e32 v96, v56
	v_mov_b32_e32 v97, v56
	v_mov_b32_e32 v98, v56
	v_mov_b32_e32 v99, v56
	v_mov_b32_e32 v100, v56
	v_mov_b32_e32 v101, v56
	v_mov_b32_e32 v102, v56
	v_mov_b32_e32 v103, v56
	v_mov_b32_e32 v104, v56
	v_mov_b32_e32 v105, v56
	v_mov_b32_e32 v106, v56
	v_mov_b32_e32 v107, v56
	v_mov_b32_e32 v108, v56
	v_mov_b32_e32 v109, v56
	v_mov_b32_e32 v110, v56
	v_mov_b32_e32 v111, v56
	v_mov_b32_e32 v112, v56
	v_mov_b32_e32 v113, v56
	v_mov_b32_e32 v114, v56
	v_mov_b32_e32 v115, v56
	s_barrier
	v_readlane_b32 s77, v253, 5
	v_readlane_b32 s82, v253, 10
	v_readlane_b32 s83, v253, 11
	v_readlane_b32 s88, v253, 16
	v_readlane_b32 s89, v253, 17
	v_readlane_b32 s90, v253, 18
	v_readlane_b32 s91, v253, 19
	s_branch .LBB0_784

.LBB0_787:
	s_andn2_b64 vcc, exec, s[20:21]
	v_mov_b32_e32 v132, v148
	v_mov_b32_e32 v153, v150
	s_cbranch_vccnz .LBB0_789
	s_waitcnt vmcnt(4)
	v_lshl_or_b32 v224, v224, 10, v167
	v_lshl_or_b32 v225, v225, 10, v167
	v_lshl_or_b32 v226, v226, 10, v167
	v_lshl_or_b32 v227, v227, 10, v167
	v_lshl_or_b32 v228, v228, 10, v167
	ds_write2st64_b32 v202, v224, v225 offset1:8
	ds_write2st64_b32 v202, v226, v227 offset0:16 offset1:24
	ds_write_b32 v202, v228 offset:8192
	s_branch .LBB0_783

.LBB0_2361:
	s_getreg_b32 s12, hwreg(HW_REG_HW_ID, 0, 6)
	s_lshl_b32 s12, s12, 2
	s_add_i32 s12, s12, 0x27000
	v_mov_b32_e32 v52, s12
	ds_read_b32 v52, v52
	v_cndmask_b32_e64 v177, 0, 1, s[20:21]
	v_mov_b32_e32 v53, v133
	v_readfirstlane_b32 s11, v177
	s_xor_b32 s50, s26, s11
	s_waitcnt lgkmcnt(0)
	v_readfirstlane_b32 s11, v52
	v_mbcnt_lo_u32_b32 v52, -1, v53
	v_mbcnt_hi_u32_b32 v52, -1, v52
	v_lshl_or_b32 v52, s11, 6, v52
	s_waitcnt vmcnt(7)
	v_cvt_pk_bf16_f32 v20, v20, v21
	v_lshrrev_b32_e32 v55, 3, v52
	v_lshlrev_b32_e32 v56, 4, v52
	v_and_b32_e32 v56, 0x70, v56
	v_mul_lo_u32 v55, v55, s38
	v_ashrrev_i32_e32 v54, 5, v52
	v_add3_u32 v57, 0, v56, v55
	ds_write_b128 v57, v[36:39]
	ds_write_b128 v57, v[32:35] offset:9216
	s_waitcnt vmcnt(6)
	ds_write_b128 v57, v[44:47] offset:18432
	s_waitcnt vmcnt(5)
	ds_write_b128 v57, v[40:43] offset:27648
	s_waitcnt vmcnt(4)
	ds_write_b128 v57, v[48:51] offset:36864
	v_lshrrev_b32_e32 v34, 1, v54
	v_bfe_u32 v32, v52, 2, 3
	v_and_b32_e32 v33, 3, v54
	v_and_b32_e32 v34, 4, v34
	v_bitop3_b32 v32, v34, v32, v33 bitop3:0x36
	v_lshlrev_b32_e32 v33, 2, v52
	v_and_b32_e32 v57, 12, v33
	v_lshlrev_b32_e32 v58, 1, v57
	v_lshl_or_b32 v59, v32, 5, v58
	v_lshlrev_b32_e32 v54, 8, v54
	v_cvt_pk_bf16_f32 v21, v22, v23
	v_add3_u32 v22, s39, v59, v54
	s_waitcnt vmcnt(6)
	v_cvt_pk_bf16_f32 v16, v16, v17
	v_cvt_pk_bf16_f32 v17, v18, v19
	ds_write2st64_b64 v22, v[20:21], v[16:17] offset1:8
	s_waitcnt vmcnt(5)
	v_cvt_pk_bf16_f32 v16, v28, v29
	v_cvt_pk_bf16_f32 v17, v30, v31
	s_waitcnt vmcnt(4)
	v_cvt_pk_bf16_f32 v18, v24, v25
	v_cvt_pk_bf16_f32 v19, v26, v27
	s_mul_i32 s11, s26, 0x2800
	ds_write2st64_b64 v22, v[16:17], v[18:19] offset0:16 offset1:24
	v_add_u32_e32 v16, s11, v174
	v_add_u32_e32 v217, s11, v168
	v_add_u32_e32 v218, 48, v16
	ds_read_b32 v132, v217
	ds_read2st64_b32 v[16:17], v218 offset0:20 offset1:28
	ds_read2st64_b32 v[22:23], v218 offset0:36 offset1:44
	v_bfe_u32 v25, v52, 2, 2
	v_bfe_u32 v26, v52, 6, 1
	s_waitcnt lgkmcnt(2)
	v_lshl_add_u64 v[18:19], v[132:133], 1, s[92:93]
	s_waitcnt lgkmcnt(1)
	v_mov_b32_e32 v132, v16
	v_lshl_add_u64 v[20:21], v[132:133], 1, s[92:93]
	v_mov_b32_e32 v132, v17
	v_lshl_add_u64 v[16:17], v[132:133], 1, s[92:93]
	s_waitcnt lgkmcnt(0)
	v_mov_b32_e32 v132, v22
	global_load_dwordx4 v[44:47], v[18:19], off offset:128
	global_load_dwordx4 v[36:39], v[20:21], off offset:128
	v_lshl_add_u64 v[18:19], v[132:133], 1, s[92:93]
	v_mov_b32_e32 v132, v23
	global_load_dwordx4 v[40:43], v[16:17], off offset:128
	global_load_dwordx4 v[32:35], v[18:19], off offset:128
	v_lshl_add_u64 v[16:17], v[132:133], 1, s[92:93]
	global_load_dwordx4 v[48:51], v[16:17], off offset:128
	v_lshrrev_b32_e32 v18, 2, v52
	v_and_b32_e32 v18, 4, v18
	v_lshrrev_b32_e32 v16, 1, v52
	v_or_b32_e32 v19, v18, v25
	v_and_b32_e32 v16, 24, v16
	v_lshlrev_b32_e32 v20, 6, v26
	v_lshlrev_b32_e32 v19, 4, v19
	v_lshlrev_b32_e32 v23, 2, v26
	v_or_b32_e32 v17, v16, v25
	v_xor_b32_e32 v19, v19, v20
	v_or_b32_e32 v26, 1, v23
	v_or_b32_e32 v27, 2, v23
	v_or_b32_e32 v23, 3, v23
	v_or_b32_e32 v19, v19, v57
	v_lshlrev_b32_e32 v17, 8, v17
	v_bitop3_b32 v26, v18, v26, v25 bitop3:0x36
	v_bitop3_b32 v27, v18, v27, v25 bitop3:0x36
	v_bitop3_b32 v18, v18, v23, v25 bitop3:0x36
	v_ashrrev_i32_e32 v53, 7, v52
	v_add_u32_e32 v20, s39, v17
	v_lshlrev_b32_e32 v19, 1, v19
	v_lshl_or_b32 v26, v26, 5, v58
	v_lshl_or_b32 v27, v27, 5, v58
	v_lshl_or_b32 v18, v18, 5, v58
	s_lshl_b32 s12, s7, 6
	v_and_b32_e32 v24, 15, v52
	v_add_u32_e32 v213, v20, v19
	v_add_u32_e32 v214, v20, v26
	v_add_u32_e32 v211, v20, v27
	v_add_u32_e32 v145, v20, v18
	v_mul_lo_u32 v20, v53, s37
	s_ashr_i32 s13, s12, 31
	v_add_u32_e32 v21, 0, v17
	v_or_b32_e32 v20, v20, v24
	s_cmpk_lt_i32 s10, 0x100
	v_add_u32_e32 v22, 0x16c00, v21
	v_lshlrev_b32_e32 v16, 1, v16
	v_mul_lo_u32 v20, v20, s38
	s_cselect_b64 s[14:15], -1, 0
	s_cmpk_gt_i32 s10, 0xff
	v_readlane_b32 s76, v253, 4
	v_add_u32_e32 v216, v22, v19
	v_add_u32_e32 v215, v22, v26
	v_add_u32_e32 v212, v22, v27
	v_add_u32_e32 v147, v22, v18
	v_add3_u32 v178, 0, v16, v20
	v_add3_u32 v16, 0, v54, v59
	v_add_u32_e32 v22, 0x18c00, v21
	s_cselect_b64 s[16:17], -1, 0
	s_ashr_i32 s11, s10, 31
	v_readlane_b32 s84, v253, 12
	v_readlane_b32 s85, v253, 13
	v_add_u32_e32 v209, 0x1b800, v16
	v_add_u32_e32 v208, 0x1c800, v16
	v_add_u32_e32 v206, 0x1d800, v16
	v_or_b32_e32 v20, 0x2000, v17
	v_add_u32_e32 v207, v22, v19
	v_add_u32_e32 v204, v22, v26
	v_add_u32_e32 v201, v22, v27
	v_add_u32_e32 v199, v22, v18
	v_add_u32_e32 v22, 0x1ac00, v21
	v_add_u32_e32 v220, 0x17800, v16
	v_add_u32_e32 v221, 0x18800, v16
	v_add_u32_e32 v222, 0x19800, v16
	v_add_u32_e32 v16, 0x1cc00, v21
	s_lshl_b64 s[18:19], s[10:11], 16
	v_add_u32_e32 v21, s49, v141
	v_readlane_b32 s86, v253, 14
	v_readlane_b32 s87, v253, 15
	v_readlane_b32 s88, v253, 16
	v_readlane_b32 s89, v253, 17
	v_readlane_b32 s90, v253, 18
	v_readlane_b32 s91, v253, 19
	s_mov_b64 s[56:57], s[84:85]
	v_add3_u32 v205, s39, v19, v20
	v_add3_u32 v203, s39, v26, v20
	v_add3_u32 v200, s39, v27, v20
	v_add3_u32 v198, s39, v18, v20
	v_add_u32_e32 v17, s40, v17
	v_add_u32_e32 v194, v22, v19
	v_add_u32_e32 v191, v22, v26
	v_add_u32_e32 v189, v22, v27
	v_add_u32_e32 v188, v22, v18
	v_add3_u32 v185, s40, v19, v20
	v_add3_u32 v183, s40, v26, v20
	v_add3_u32 v181, s40, v27, v20
	v_add3_u32 v179, s40, v18, v20
	v_add_u32_e32 v20, -1, v176
	s_cmpk_lt_i32 s6, 0x100
	v_add_u32_e32 v22, 0x80, v21
	s_mov_b64 s[58:59], s[86:87]
	v_add_u32_e32 v187, v17, v18
	v_add_u32_e32 v186, v16, v19
	v_add_u32_e32 v184, v16, v26
	v_add_u32_e32 v182, v16, v27
	v_add_u32_e32 v180, v16, v18
	v_min_i32_e32 v16, v21, v20
	v_add_u32_e32 v18, 64, v21
	v_min_i32_e32 v148, v22, v20
	v_add_u32_e32 v22, 0xc0, v21
	v_add_u32_e32 v21, 0x100, v21
	s_cselect_b32 s22, s6, 1
	s_cselect_b32 s53, s27, s56
	s_cselect_b32 s54, s28, s57
	s_cselect_b32 s56, s33, s59
	v_min_i32_e32 v18, v18, v20
	v_min_i32_e32 v150, v22, v20
	v_min_i32_e32 v152, v21, v20
	s_cselect_b32 s55, s29, s58
	s_ashr_i32 s23, s22, 31
	v_mov_b32_e32 v20, s56
	v_mov_b32_e32 v21, s54
	s_lshl_b64 s[22:23], s[22:23], 20
	v_cndmask_b32_e64 v21, v20, v21, s[4:5]
	v_mov_b32_e32 v20, s55
	v_readlane_b32 s54, v253, 61
	v_readlane_b32 s55, v253, 62
	s_add_u32 s18, s54, s18
	v_add_u32_e32 v193, v17, v19
	v_add_u32_e32 v190, v17, v26
	v_add_u32_e32 v192, v17, v27
	v_ashrrev_i32_e32 v17, 31, v16
	v_ashrrev_i32_e32 v19, 31, v18
	v_ashrrev_i32_e32 v149, 31, v148
	v_ashrrev_i32_e32 v151, 31, v150
	v_ashrrev_i32_e32 v153, 31, v152
	s_addc_u32 s19, s55, s19
	v_mov_b32_e32 v22, s53
	v_lshl_add_u64 v[154:155], v[16:17], 2, s[18:19]
	v_lshl_add_u64 v[156:157], v[18:19], 2, s[18:19]
	v_lshl_add_u64 v[158:159], v[148:149], 2, s[18:19]
	v_lshl_add_u64 v[160:161], v[150:151], 2, s[18:19]
	v_lshl_add_u64 v[162:163], v[152:153], 2, s[18:19]
	s_and_b64 s[98:99], s[20:21], s[14:15]
	s_cbranch_scc0 .Lopt1_m11_skip
	global_load_dword v224, v[154:155], off
	global_load_dword v225, v[156:157], off
	global_load_dword v226, v[158:159], off
	global_load_dword v227, v[160:161], off
	global_load_dword v228, v[162:163], off
.Lopt1_m11_skip:
	s_lshl_b64 s[18:19], s[12:13], 2
	v_cndmask_b32_e64 v20, v20, v22, s[4:5]
	s_add_u32 s18, s22, s18
	v_add3_u32 v195, 0, v55, v56
	s_mul_i32 s51, s50, 0x2800
	v_lshl_or_b32 v149, v16, 10, v167
	v_lshl_add_u64 v[16:17], v[20:21], 0, v[142:143]
	s_addc_u32 s19, s23, s19
	v_mov_b32_e32 v52, 0
	s_mov_b32 s52, 0
	v_add3_u32 v210, s40, v54, v59
	v_add_u32_e32 v196, 0x12000, v195
	v_add_u32_e32 v197, 0x14400, v195
	v_add3_u32 v219, s39, v54, v59
	v_add_u32_e32 v202, s51, v168
	v_lshl_or_b32 v151, v18, 10, v167
	v_lshl_add_u64 v[164:165], v[16:17], 0, s[18:19]
	s_mov_b64 s[18:19], 0
	s_xor_b64 s[20:21], s[20:21], -1
	v_mov_b32_e32 v53, v52
	v_mov_b32_e32 v54, v52
	v_mov_b32_e32 v55, v52
	v_mov_b32_e32 v56, v52
	v_mov_b32_e32 v57, v52
	v_mov_b32_e32 v58, v52
	v_mov_b32_e32 v59, v52
	v_mov_b32_e32 v64, v52
	v_mov_b32_e32 v65, v52
	v_mov_b32_e32 v66, v52
	v_mov_b32_e32 v67, v52
	v_mov_b32_e32 v80, v52
	v_mov_b32_e32 v81, v52
	v_mov_b32_e32 v82, v52
	v_mov_b32_e32 v83, v52
	v_mov_b32_e32 v76, v52
	v_mov_b32_e32 v77, v52
	v_mov_b32_e32 v78, v52
	v_mov_b32_e32 v79, v52
	v_mov_b32_e32 v68, v52
	v_mov_b32_e32 v69, v52
	v_mov_b32_e32 v70, v52
	v_mov_b32_e32 v71, v52
	v_mov_b32_e32 v60, v52
	v_mov_b32_e32 v61, v52
	v_mov_b32_e32 v62, v52
	v_mov_b32_e32 v63, v52
	v_mov_b32_e32 v72, v52
	v_mov_b32_e32 v73, v52
	v_mov_b32_e32 v74, v52
	v_mov_b32_e32 v75, v52
	v_mov_b32_e32 v84, v52
	v_mov_b32_e32 v85, v52
	v_mov_b32_e32 v86, v52
	v_mov_b32_e32 v87, v52
	v_mov_b32_e32 v24, v52
	v_mov_b32_e32 v25, v52
	v_mov_b32_e32 v26, v52
	v_mov_b32_e32 v27, v52
	v_mov_b32_e32 v28, v52
	v_mov_b32_e32 v29, v52
	v_mov_b32_e32 v30, v52
	v_mov_b32_e32 v31, v52
	v_mov_b32_e32 v88, v52
	v_mov_b32_e32 v89, v52
	v_mov_b32_e32 v90, v52
	v_mov_b32_e32 v91, v52
	v_mov_b32_e32 v16, v52
	v_mov_b32_e32 v17, v52
	v_mov_b32_e32 v18, v52
	v_mov_b32_e32 v19, v52
	v_mov_b32_e32 v20, v52
	v_mov_b32_e32 v21, v52
	v_mov_b32_e32 v22, v52
	v_mov_b32_e32 v23, v52
	v_mov_b32_e32 v92, v52
	v_mov_b32_e32 v93, v52
	v_mov_b32_e32 v94, v52
	v_mov_b32_e32 v95, v52
	v_mov_b32_e32 v96, v52
	v_mov_b32_e32 v97, v52
	v_mov_b32_e32 v98, v52
	v_mov_b32_e32 v99, v52
	v_mov_b32_e32 v100, v52
	v_mov_b32_e32 v101, v52
	v_mov_b32_e32 v102, v52
	v_mov_b32_e32 v103, v52
	v_mov_b32_e32 v104, v52
	v_mov_b32_e32 v105, v52
	v_mov_b32_e32 v106, v52
	v_mov_b32_e32 v107, v52
	v_mov_b32_e32 v108, v52
	v_mov_b32_e32 v109, v52
	v_mov_b32_e32 v110, v52
	v_mov_b32_e32 v111, v52
	v_mov_b32_e32 v112, v52
	v_mov_b32_e32 v113, v52
	v_mov_b32_e32 v114, v52
	v_mov_b32_e32 v115, v52
	s_barrier
	v_readlane_b32 s77, v253, 5
	v_readlane_b32 s78, v253, 6
	v_readlane_b32 s79, v253, 7
	v_readlane_b32 s80, v253, 8
	v_readlane_b32 s81, v253, 9
	v_readlane_b32 s82, v253, 10
	v_readlane_b32 s83, v253, 11
	s_mov_b64 s[60:61], s[88:89]
	s_mov_b64 s[62:63], s[90:91]
	s_branch .LBB0_2364

.LBB0_2367:
	s_andn2_b64 vcc, exec, s[22:23]
	v_mov_b32_e32 v132, v148
	v_mov_b32_e32 v153, v150
	s_cbranch_vccnz .LBB0_2369
	s_waitcnt vmcnt(4)
	v_lshl_or_b32 v224, v224, 10, v167
	v_lshl_or_b32 v225, v225, 10, v167
	v_lshl_or_b32 v226, v226, 10, v167
	v_lshl_or_b32 v227, v227, 10, v167
	v_lshl_or_b32 v228, v228, 10, v167
	ds_write2st64_b32 v202, v224, v225 offset1:8
	ds_write2st64_b32 v202, v226, v227 offset0:16 offset1:24
	ds_write_b32 v202, v228 offset:8192
	s_branch .LBB0_2363
